# baseline (speedup 1.0000x reference)
.LBB0_34:
	s_or_b64 exec, exec, s[4:5]
	s_mov_b64 s[18:19], s[62:63]
	v_cmp_le_i32_e32 vcc, s36, v106
	s_and_saveexec_b64 s[2:3], vcc
	s_xor_b64 s[2:3], exec, s[2:3]
	v_lshlrev_b32_e32 v107, 4, v82
	s_or_saveexec_b64 s[2:3], s[2:3]
	v_mov_b32_e32 v10, 0
	v_mov_b32_e32 v11, v10
	v_mov_b32_e32 v12, v10
	v_mov_b32_e32 v13, v10
	v_mov_b64_e32 v[6:7], v[10:11]
	v_mov_b64_e32 v[8:9], v[12:13]
	s_xor_b64 exec, exec, s[2:3]
	s_cbranch_execz .LBB0_38
	v_lshl_or_b32 v6, v14, 8, v107
	s_waitcnt lgkmcnt(0)
	global_load_dwordx4 v[6:9], v6, s[18:19] sc1
.LBB0_38:
	s_or_b64 exec, exec, s[2:3]
	s_mov_b64 s[28:29], s[64:65]
	s_add_i32 s2, s36, -4
	v_cmp_gt_i32_e32 vcc, s2, v106
	s_and_saveexec_b64 s[2:3], vcc
	s_cbranch_execz .LBB0_40
	v_lshl_or_b32 v10, v15, 8, v107
	s_waitcnt lgkmcnt(0)
	global_load_dwordx4 v[10:13], v10, s[18:19] sc1

.LBB0_81:
	s_or_b64 exec, exec, s[0:1]
	v_cmp_gt_i32_e32 vcc, s26, v106
	s_and_saveexec_b64 s[0:1], vcc
	s_cbranch_execz .LBB0_83
	s_waitcnt lgkmcnt(0)
	v_lshl_or_b32 v6, v14, 8, v107
	global_load_dwordx4 v[6:9], v6, s[18:19] sc1
.LBB0_83:
	s_or_b64 exec, exec, s[0:1]
	v_mov_b32_e32 v63, v62
	v_mov_b32_e32 v64, v62
	v_mov_b32_e32 v65, v62
	v_mov_b64_e32 v[10:11], v[62:63]
	v_cmp_gt_i32_e32 vcc, s26, v112
	v_mov_b64_e32 v[12:13], v[64:65]
	s_and_saveexec_b64 s[0:1], vcc
	s_cbranch_execz .LBB0_85
	s_waitcnt lgkmcnt(0)
	v_lshl_or_b32 v10, v15, 8, v107
	global_load_dwordx4 v[10:13], v10, s[18:19] sc1
